# v27 + gate-GEMM epilogue parameters read once per tile + next-layer weight prep (int8 W_in/W_g) column-max and quantise passes with 16 requests in flight
# speedup vs baseline: 1.0050x; 1.0050x over previous
.LBB0_978:
	v_add_u32_e32 v132, s21, v1
	v_ashrrev_i32_e32 v133, 31, v132
	v_add_u32_e32 v170, 16, v132
	v_lshl_add_u64 v[134:135], v[132:133], 2, s[8:9]
	v_ashrrev_i32_e32 v171, 31, v170
	v_add_u32_e32 v168, 32, v132
	global_load_dword v179, v[134:135], off
	v_lshl_add_u64 v[134:135], v[170:171], 2, s[8:9]
	v_ashrrev_i32_e32 v169, 31, v168
	v_add_u32_e32 v166, 48, v132
	global_load_dword v171, v[134:135], off
	v_lshl_add_u64 v[134:135], v[168:169], 2, s[8:9]
	v_ashrrev_i32_e32 v167, 31, v166
	v_add_u32_e32 v164, 0x80, v132
	v_mov_b64_e32 v[156:157], s[4:5]
	s_movk_i32 s24, 0xc00
	global_load_dword v169, v[134:135], off
	v_lshl_add_u64 v[134:135], v[166:167], 2, s[8:9]
	v_ashrrev_i32_e32 v165, 31, v164
	v_add_u32_e32 v162, 0x90, v132
	v_add_u32_e32 v160, 0xa0, v132
	v_add_u32_e32 v154, 0xb0, v132
	s_ashr_i32 s21, s20, 31
	v_mad_i64_i32 v[132:133], s[22:23], v132, s24, v[156:157]
	global_load_dword v167, v[134:135], off
	v_lshl_add_u64 v[134:135], v[164:165], 2, s[8:9]
	v_ashrrev_i32_e32 v163, 31, v162
	v_add_u32_e32 v174, s20, v177
	v_lshl_add_u64 v[132:133], v[132:133], 0, s[20:21]
	global_load_dword v165, v[134:135], off
	v_lshl_add_u64 v[134:135], v[162:163], 2, s[8:9]
	v_ashrrev_i32_e32 v161, 31, v160
	v_lshl_add_u64 v[132:133], v[132:133], 0, s[12:13]
	v_ashrrev_i32_e32 v175, 31, v174
	global_load_dword v163, v[134:135], off
	v_lshl_add_u64 v[134:135], v[160:161], 2, s[8:9]
	v_ashrrev_i32_e32 v155, 31, v154
	v_lshl_add_u64 v[172:173], v[132:133], 0, v[150:151]
	v_lshlrev_b64 v[132:133], 2, v[174:175]
	global_load_dword v161, v[134:135], off
	v_lshl_add_u64 v[134:135], v[154:155], 2, s[8:9]
	v_lshl_add_u64 v[158:159], s[10:11], 0, v[132:133]
	global_load_dword v155, v[134:135], off
	v_lshl_add_u64 v[152:153], s[6:7], 0, v[132:133]
	global_load_dwordx4 v[188:191], v[158:159], off offset:16
	global_load_dwordx4 v[192:195], v[158:159], off
	global_load_dwordx4 v[196:199], v[152:153], off offset:16
	global_load_dwordx4 v[200:203], v[152:153], off
	global_load_dwordx4 v[204:207], v[158:159], off offset:528
	global_load_dwordx4 v[208:211], v[158:159], off offset:512
	global_load_dwordx4 v[212:215], v[152:153], off offset:528
	global_load_dwordx4 v[216:219], v[152:153], off offset:512
	v_cvt_f32_i32_e32 v124, v124
	v_cvt_f32_i32_e32 v125, v125
	v_cvt_f32_i32_e32 v126, v126
	v_cvt_f32_i32_e32 v128, v128
	v_cvt_f32_i32_e32 v127, v127
	v_cvt_f32_i32_e32 v116, v116
	v_cvt_f32_i32_e32 v117, v117
	v_cvt_f32_i32_e32 v118, v118
	v_cvt_f32_i32_e32 v120, v120
	v_cvt_f32_i32_e32 v119, v119
	v_cvt_f32_i32_e32 v108, v108
	v_cvt_f32_i32_e32 v109, v109
	v_cvt_f32_i32_e32 v110, v110
	v_cvt_f32_i32_e32 v112, v112
	v_cvt_f32_i32_e32 v111, v111
	v_cvt_f32_i32_e32 v100, v100
	v_cvt_f32_i32_e32 v101, v101
	v_cvt_f32_i32_e32 v102, v102
	v_cvt_f32_i32_e32 v104, v104
	v_cvt_f32_i32_e32 v103, v103
	v_cvt_f32_i32_e32 v92, v92
	v_cvt_f32_i32_e32 v93, v93
	v_cvt_f32_i32_e32 v94, v94
	v_cvt_f32_i32_e32 v96, v96
	v_cvt_f32_i32_e32 v95, v95
	v_cvt_f32_i32_e32 v84, v84
	v_cvt_f32_i32_e32 v85, v85
	v_cvt_f32_i32_e32 v86, v86
	v_cvt_f32_i32_e32 v88, v88
	v_cvt_f32_i32_e32 v87, v87
	v_cvt_f32_i32_e32 v76, v76
	v_cvt_f32_i32_e32 v77, v77
	v_cvt_f32_i32_e32 v78, v78
	v_cvt_f32_i32_e32 v80, v80
	v_cvt_f32_i32_e32 v79, v79
	v_cvt_f32_i32_e32 v68, v68
	v_cvt_f32_i32_e32 v69, v69
	v_cvt_f32_i32_e32 v70, v70
	v_cvt_f32_i32_e32 v72, v72
	v_cvt_f32_i32_e32 v71, v71
	v_cvt_f32_i32_e32 v60, v60
	v_cvt_f32_i32_e32 v61, v61
	v_cvt_f32_i32_e32 v62, v62
	v_cvt_f32_i32_e32 v64, v64
	v_cvt_f32_i32_e32 v63, v63
	v_cvt_f32_i32_e32 v52, v52
	v_cvt_f32_i32_e32 v53, v53
	v_cvt_f32_i32_e32 v54, v54
	v_cvt_f32_i32_e32 v56, v56
	v_cvt_f32_i32_e32 v55, v55
	v_cvt_f32_i32_e32 v44, v44
	v_cvt_f32_i32_e32 v45, v45
	v_cvt_f32_i32_e32 v46, v46
	v_cvt_f32_i32_e32 v48, v48
	v_cvt_f32_i32_e32 v47, v47
	v_cvt_f32_i32_e32 v36, v36
	v_cvt_f32_i32_e32 v37, v37
	v_cvt_f32_i32_e32 v38, v38
	v_cvt_f32_i32_e32 v40, v40
	v_cvt_f32_i32_e32 v39, v39
	v_cvt_f32_i32_e32 v28, v28
	v_cvt_f32_i32_e32 v29, v29
	v_cvt_f32_i32_e32 v30, v30
	v_cvt_f32_i32_e32 v32, v32
	v_cvt_f32_i32_e32 v31, v31
	v_cvt_f32_i32_e32 v20, v20
	v_cvt_f32_i32_e32 v21, v21
	v_cvt_f32_i32_e32 v22, v22
	v_cvt_f32_i32_e32 v24, v24
	v_cvt_f32_i32_e32 v23, v23
	v_cvt_f32_i32_e32 v12, v12
	v_cvt_f32_i32_e32 v13, v13
	v_cvt_f32_i32_e32 v14, v14
	v_cvt_f32_i32_e32 v16, v16
	v_cvt_f32_i32_e32 v15, v15
	v_cvt_f32_i32_e32 v4, v4
	s_waitcnt vmcnt(0)
	v_mov_b64_e32 v[132:133], v[188:189]
	v_mov_b64_e32 v[134:135], v[190:191]
	v_mov_b64_e32 v[180:181], v[192:193]
	v_mov_b64_e32 v[182:183], v[194:195]
	v_mov_b64_e32 v[136:137], v[196:197]
	v_mov_b64_e32 v[138:139], v[198:199]
	v_mov_b64_e32 v[184:185], v[200:201]
	v_mov_b64_e32 v[186:187], v[202:203]
	v_mul_f32_e32 v132, v179, v132
	v_mul_f32_e32 v175, v179, v180
	v_fma_f32 v124, v132, v124, v136
	v_mul_f32_e32 v124, 0xbfb8aa3b, v124
	v_exp_f32_e32 v124, v124
	v_fma_f32 v128, v175, v128, v184
	v_mul_f32_e32 v128, 0xbfb8aa3b, v128
	v_exp_f32_e32 v128, v128
	v_add_f32_e32 v124, 1.0, v124
	v_rcp_f32_e32 v132, v124
	v_cvt_f32_i32_e32 v124, v129
	v_mul_f32_e32 v129, v179, v181
	v_add_f32_e32 v128, 1.0, v128
	v_rcp_f32_e32 v128, v128
	v_fma_f32 v124, v129, v124, v185
	v_mul_f32_e32 v129, v179, v133
	v_fma_f32 v125, v129, v125, v137
	v_cvt_f32_i32_e32 v129, v130
	v_mul_f32_e32 v130, v179, v182
	v_mul_f32_e32 v124, 0xbfb8aa3b, v124
	v_exp_f32_e32 v124, v124
	v_fma_f32 v129, v130, v129, v186
	v_mul_f32_e32 v130, v179, v134
	v_fma_f32 v126, v130, v126, v138
	v_cvt_f32_i32_e32 v130, v131
	v_mul_f32_e32 v131, v179, v183
	v_mul_f32_e32 v129, 0xbfb8aa3b, v129
	v_exp_f32_e32 v129, v129
	v_fmac_f32_e32 v187, v131, v130
	v_mul_f32_e32 v130, 0xbfb8aa3b, v187
	v_exp_f32_e32 v130, v130
	v_mul_f32_e32 v125, 0xbfb8aa3b, v125
	v_mul_f32_e32 v131, v179, v135
	v_add_f32_e32 v124, 1.0, v124
	v_exp_f32_e32 v125, v125
	v_mul_f32_e32 v126, 0xbfb8aa3b, v126
	v_fmac_f32_e32 v139, v131, v127
	v_rcp_f32_e32 v124, v124
	v_add_f32_e32 v129, 1.0, v129
	v_exp_f32_e32 v126, v126
	v_mul_f32_e32 v127, 0xbfb8aa3b, v139
	v_rcp_f32_e32 v129, v129
	v_add_f32_e32 v130, 1.0, v130
	v_exp_f32_e32 v127, v127
	v_rcp_f32_e32 v130, v130
	v_add_f32_e32 v125, 1.0, v125
	v_mul_f32_e32 v128, 0x437f0000, v128
	v_rcp_f32_e32 v125, v125
	v_add_f32_e32 v126, 1.0, v126
	v_cvt_pk_u8_f32 v128, v128, 0, 0
	v_mul_f32_e32 v124, 0x437f0000, v124
	v_rcp_f32_e32 v126, v126
	v_add_f32_e32 v127, 1.0, v127
	v_cvt_pk_u8_f32 v124, v124, 1, v128
	v_mul_f32_e32 v128, 0x437f0000, v129
	v_rcp_f32_e32 v127, v127
	v_cvt_pk_u8_f32 v124, v128, 2, v124
	v_mul_f32_e32 v128, 0x437f0000, v130
	v_cvt_pk_u8_f32 v124, v128, 3, v124
	v_mul_f32_e32 v128, 0x437f0000, v132
	v_cvt_pk_u8_f32 v128, v128, 0, 0
	v_mul_f32_e32 v125, 0x437f0000, v125
	v_cvt_pk_u8_f32 v125, v125, 1, v128
	v_mul_f32_e32 v126, 0x437f0000, v126
	v_cvt_pk_u8_f32 v125, v126, 2, v125
	v_mul_f32_e32 v126, 0x437f0000, v127
	v_cvt_pk_u8_f32 v125, v126, 3, v125
	global_store_dwordx2 v[172:173], v[124:125], off
	v_add_u32_e32 v124, 0x80, v174
	v_ashrrev_i32_e32 v125, 31, v124
	v_lshl_add_u64 v[132:133], v[124:125], 2, s[10:11]
	v_mov_b64_e32 v[128:129], v[204:205]
	v_mov_b64_e32 v[130:131], v[206:207]
	v_mov_b64_e32 v[134:135], v[208:209]
	v_mov_b64_e32 v[136:137], v[210:211]
	v_mov_b64_e32 v[124:125], v[212:213]
	v_mov_b64_e32 v[126:127], v[214:215]
	v_mov_b64_e32 v[180:181], v[216:217]
	v_mov_b64_e32 v[182:183], v[218:219]
	v_cvt_f32_i32_e32 v5, v5
	v_cvt_f32_i32_e32 v6, v6
	v_cvt_f32_i32_e32 v8, v8
	v_cvt_f32_i32_e32 v7, v7
	s_movk_i32 s84, 0xc00
	s_andn2_b64 vcc, exec, s[2:3]
	s_mov_b32 s55, 0xda24260
	v_mul_f32_e32 v128, v179, v128
	v_mul_f32_e32 v134, v179, v134
	v_fma_f32 v116, v128, v116, v124
	v_mul_f32_e32 v116, 0xbfb8aa3b, v116
	v_exp_f32_e32 v116, v116
	v_fma_f32 v120, v134, v120, v180
	v_mul_f32_e32 v120, 0xbfb8aa3b, v120
	v_exp_f32_e32 v120, v120
	v_add_f32_e32 v116, 1.0, v116
	v_rcp_f32_e32 v124, v116
	v_cvt_f32_i32_e32 v116, v121
	v_mul_f32_e32 v121, v179, v135
	v_add_f32_e32 v120, 1.0, v120
	v_rcp_f32_e32 v120, v120
	v_fma_f32 v116, v121, v116, v181
	v_mul_f32_e32 v121, v179, v129
	v_fma_f32 v117, v121, v117, v125
	v_cvt_f32_i32_e32 v121, v122
	v_mul_f32_e32 v122, v179, v136
	v_mul_f32_e32 v116, 0xbfb8aa3b, v116
	v_exp_f32_e32 v116, v116
	v_fma_f32 v121, v122, v121, v182
	v_mul_f32_e32 v122, v179, v130
	v_fma_f32 v118, v122, v118, v126
	v_cvt_f32_i32_e32 v122, v123
	v_mul_f32_e32 v123, v179, v137
	v_mul_f32_e32 v121, 0xbfb8aa3b, v121
	v_exp_f32_e32 v121, v121
	v_fmac_f32_e32 v183, v123, v122
	v_mul_f32_e32 v122, 0xbfb8aa3b, v183
	v_exp_f32_e32 v122, v122
	v_mul_f32_e32 v117, 0xbfb8aa3b, v117
	v_mul_f32_e32 v123, v179, v131
	v_add_f32_e32 v116, 1.0, v116
	v_exp_f32_e32 v117, v117
	v_mul_f32_e32 v118, 0xbfb8aa3b, v118
	v_fmac_f32_e32 v127, v123, v119
	v_rcp_f32_e32 v116, v116
	v_add_f32_e32 v121, 1.0, v121
	v_exp_f32_e32 v118, v118
	v_mul_f32_e32 v119, 0xbfb8aa3b, v127
	v_rcp_f32_e32 v121, v121
	v_add_f32_e32 v122, 1.0, v122
	v_exp_f32_e32 v119, v119
	v_rcp_f32_e32 v122, v122
	v_add_f32_e32 v117, 1.0, v117
	v_mul_f32_e32 v120, 0x437f0000, v120
	v_rcp_f32_e32 v117, v117
	v_add_f32_e32 v118, 1.0, v118
	v_cvt_pk_u8_f32 v120, v120, 0, 0
	v_mul_f32_e32 v116, 0x437f0000, v116
	v_rcp_f32_e32 v118, v118
	v_add_f32_e32 v119, 1.0, v119
	v_cvt_pk_u8_f32 v116, v116, 1, v120
	v_mul_f32_e32 v120, 0x437f0000, v121
	v_rcp_f32_e32 v119, v119
	v_cvt_pk_u8_f32 v116, v120, 2, v116
	v_mul_f32_e32 v120, 0x437f0000, v122
	v_cvt_pk_u8_f32 v116, v120, 3, v116
	v_mul_f32_e32 v120, 0x437f0000, v124
	v_cvt_pk_u8_f32 v120, v120, 0, 0
	v_mul_f32_e32 v117, 0x437f0000, v117
	v_cvt_pk_u8_f32 v117, v117, 1, v120
	v_mul_f32_e32 v118, 0x437f0000, v118
	v_cvt_pk_u8_f32 v117, v118, 2, v117
	v_mul_f32_e32 v118, 0x437f0000, v119
	v_cvt_pk_u8_f32 v117, v118, 3, v117
	global_store_dwordx2 v[172:173], v[116:117], off offset:128
	v_mad_i64_i32 v[116:117], s[22:23], v170, s24, v[156:157]
	v_lshl_add_u64 v[116:117], v[116:117], 0, s[20:21]
	v_lshl_add_u64 v[116:117], v[116:117], 0, s[12:13]
	v_lshl_add_u64 v[124:125], v[116:117], 0, v[150:151]
	v_mov_b64_e32 v[120:121], v[188:189]
	v_mov_b64_e32 v[122:123], v[190:191]
	v_mov_b64_e32 v[126:127], v[192:193]
	v_mov_b64_e32 v[128:129], v[194:195]
	v_mov_b64_e32 v[116:117], v[196:197]
	v_mov_b64_e32 v[118:119], v[198:199]
	v_mov_b64_e32 v[134:135], v[200:201]
	v_mov_b64_e32 v[136:137], v[202:203]
	v_mul_f32_e32 v120, v171, v120
	v_mul_f32_e32 v126, v171, v126
	v_fma_f32 v108, v120, v108, v116
	v_mul_f32_e32 v108, 0xbfb8aa3b, v108
	v_exp_f32_e32 v108, v108
	v_fma_f32 v112, v126, v112, v134
	v_mul_f32_e32 v112, 0xbfb8aa3b, v112
	v_exp_f32_e32 v112, v112
	v_add_f32_e32 v108, 1.0, v108
	v_rcp_f32_e32 v116, v108
	v_cvt_f32_i32_e32 v108, v113
	v_mul_f32_e32 v113, v171, v127
	v_add_f32_e32 v112, 1.0, v112
	v_rcp_f32_e32 v112, v112
	v_fma_f32 v108, v113, v108, v135
	v_mul_f32_e32 v113, v171, v121
	v_fma_f32 v109, v113, v109, v117
	v_cvt_f32_i32_e32 v113, v114
	v_mul_f32_e32 v114, v171, v128
	v_mul_f32_e32 v108, 0xbfb8aa3b, v108
	v_exp_f32_e32 v108, v108
	v_fma_f32 v113, v114, v113, v136
	v_mul_f32_e32 v114, v171, v122
	v_fma_f32 v110, v114, v110, v118
	v_cvt_f32_i32_e32 v114, v115
	v_mul_f32_e32 v115, v171, v129
	v_mul_f32_e32 v113, 0xbfb8aa3b, v113
	v_exp_f32_e32 v113, v113
	v_fmac_f32_e32 v137, v115, v114
	v_mul_f32_e32 v114, 0xbfb8aa3b, v137
	v_exp_f32_e32 v114, v114
	v_mul_f32_e32 v109, 0xbfb8aa3b, v109
	v_mul_f32_e32 v115, v171, v123
	v_add_f32_e32 v108, 1.0, v108
	v_exp_f32_e32 v109, v109
	v_mul_f32_e32 v110, 0xbfb8aa3b, v110
	v_fmac_f32_e32 v119, v115, v111
	v_rcp_f32_e32 v108, v108
	v_add_f32_e32 v113, 1.0, v113
	v_exp_f32_e32 v110, v110
	v_mul_f32_e32 v111, 0xbfb8aa3b, v119
	v_rcp_f32_e32 v113, v113
	v_add_f32_e32 v114, 1.0, v114
	v_exp_f32_e32 v111, v111
	v_rcp_f32_e32 v114, v114
	v_add_f32_e32 v109, 1.0, v109
	v_mul_f32_e32 v112, 0x437f0000, v112
	v_rcp_f32_e32 v109, v109
	v_add_f32_e32 v110, 1.0, v110
	v_cvt_pk_u8_f32 v112, v112, 0, 0
	v_mul_f32_e32 v108, 0x437f0000, v108
	v_rcp_f32_e32 v110, v110
	v_add_f32_e32 v111, 1.0, v111
	v_cvt_pk_u8_f32 v108, v108, 1, v112
	v_mul_f32_e32 v112, 0x437f0000, v113
	v_rcp_f32_e32 v111, v111
	v_cvt_pk_u8_f32 v108, v112, 2, v108
	v_mul_f32_e32 v112, 0x437f0000, v114
	v_cvt_pk_u8_f32 v108, v112, 3, v108
	v_mul_f32_e32 v112, 0x437f0000, v116
	v_cvt_pk_u8_f32 v112, v112, 0, 0
	v_mul_f32_e32 v109, 0x437f0000, v109
	v_cvt_pk_u8_f32 v109, v109, 1, v112
	v_mul_f32_e32 v110, 0x437f0000, v110
	v_cvt_pk_u8_f32 v109, v110, 2, v109
	v_mul_f32_e32 v110, 0x437f0000, v111
	v_cvt_pk_u8_f32 v109, v110, 3, v109
	global_store_dwordx2 v[124:125], v[108:109], off
	v_mov_b64_e32 v[112:113], v[204:205]
	v_mov_b64_e32 v[114:115], v[206:207]
	v_mov_b64_e32 v[116:117], v[208:209]
	v_mov_b64_e32 v[118:119], v[210:211]
	s_nop 0
	v_mov_b64_e32 v[108:109], v[212:213]
	v_mov_b64_e32 v[110:111], v[214:215]
	v_mov_b64_e32 v[120:121], v[216:217]
	v_mov_b64_e32 v[122:123], v[218:219]
	v_mul_f32_e32 v112, v171, v112
	v_mul_f32_e32 v116, v171, v116
	v_fma_f32 v100, v112, v100, v108
	v_mul_f32_e32 v100, 0xbfb8aa3b, v100
	v_exp_f32_e32 v100, v100
	v_fma_f32 v104, v116, v104, v120
	v_mul_f32_e32 v104, 0xbfb8aa3b, v104
	v_exp_f32_e32 v104, v104
	v_add_f32_e32 v100, 1.0, v100
	v_rcp_f32_e32 v108, v100
	v_cvt_f32_i32_e32 v100, v105
	v_mul_f32_e32 v105, v171, v117
	v_add_f32_e32 v104, 1.0, v104
	v_rcp_f32_e32 v104, v104
	v_fma_f32 v100, v105, v100, v121
	v_mul_f32_e32 v105, v171, v113
	v_fma_f32 v101, v105, v101, v109
	v_cvt_f32_i32_e32 v105, v106
	v_mul_f32_e32 v106, v171, v118
	v_mul_f32_e32 v100, 0xbfb8aa3b, v100
	v_exp_f32_e32 v100, v100
	v_fma_f32 v105, v106, v105, v122
	v_mul_f32_e32 v106, v171, v114
	v_fma_f32 v102, v106, v102, v110
	v_cvt_f32_i32_e32 v106, v107
	v_mul_f32_e32 v107, v171, v119
	v_mul_f32_e32 v105, 0xbfb8aa3b, v105
	v_exp_f32_e32 v105, v105
	v_fmac_f32_e32 v123, v107, v106
	v_mul_f32_e32 v106, 0xbfb8aa3b, v123
	v_exp_f32_e32 v106, v106
	v_mul_f32_e32 v101, 0xbfb8aa3b, v101
	v_mul_f32_e32 v107, v171, v115
	v_add_f32_e32 v100, 1.0, v100
	v_exp_f32_e32 v101, v101
	v_mul_f32_e32 v102, 0xbfb8aa3b, v102
	v_fmac_f32_e32 v111, v107, v103
	v_rcp_f32_e32 v100, v100
	v_add_f32_e32 v105, 1.0, v105
	v_exp_f32_e32 v102, v102
	v_mul_f32_e32 v103, 0xbfb8aa3b, v111
	v_rcp_f32_e32 v105, v105
	v_add_f32_e32 v106, 1.0, v106
	v_exp_f32_e32 v103, v103
	v_rcp_f32_e32 v106, v106
	v_add_f32_e32 v101, 1.0, v101
	v_mul_f32_e32 v104, 0x437f0000, v104
	v_rcp_f32_e32 v101, v101
	v_add_f32_e32 v102, 1.0, v102
	v_cvt_pk_u8_f32 v104, v104, 0, 0
	v_mul_f32_e32 v100, 0x437f0000, v100
	v_rcp_f32_e32 v102, v102
	v_add_f32_e32 v103, 1.0, v103
	v_cvt_pk_u8_f32 v100, v100, 1, v104
	v_mul_f32_e32 v104, 0x437f0000, v105
	v_rcp_f32_e32 v103, v103
	v_cvt_pk_u8_f32 v100, v104, 2, v100
	v_mul_f32_e32 v104, 0x437f0000, v106
	v_cvt_pk_u8_f32 v100, v104, 3, v100
	v_mul_f32_e32 v104, 0x437f0000, v108
	v_cvt_pk_u8_f32 v104, v104, 0, 0
	v_mul_f32_e32 v101, 0x437f0000, v101
	v_cvt_pk_u8_f32 v101, v101, 1, v104
	v_mul_f32_e32 v102, 0x437f0000, v102
	v_cvt_pk_u8_f32 v101, v102, 2, v101
	v_mul_f32_e32 v102, 0x437f0000, v103
	v_cvt_pk_u8_f32 v101, v102, 3, v101
	global_store_dwordx2 v[124:125], v[100:101], off offset:128
	v_mad_i64_i32 v[100:101], s[22:23], v168, s24, v[156:157]
	v_lshl_add_u64 v[100:101], v[100:101], 0, s[20:21]
	v_lshl_add_u64 v[100:101], v[100:101], 0, s[12:13]
	v_lshl_add_u64 v[108:109], v[100:101], 0, v[150:151]
	v_mov_b64_e32 v[104:105], v[188:189]
	v_mov_b64_e32 v[106:107], v[190:191]
	v_mov_b64_e32 v[110:111], v[192:193]
	v_mov_b64_e32 v[112:113], v[194:195]
	v_mov_b64_e32 v[100:101], v[196:197]
	v_mov_b64_e32 v[102:103], v[198:199]
	v_mov_b64_e32 v[114:115], v[200:201]
	v_mov_b64_e32 v[116:117], v[202:203]
	v_mul_f32_e32 v104, v169, v104
	v_mul_f32_e32 v110, v169, v110
	v_fma_f32 v92, v104, v92, v100
	v_mul_f32_e32 v92, 0xbfb8aa3b, v92
	v_exp_f32_e32 v92, v92
	v_fma_f32 v96, v110, v96, v114
	v_mul_f32_e32 v96, 0xbfb8aa3b, v96
	v_exp_f32_e32 v96, v96
	v_add_f32_e32 v92, 1.0, v92
	v_rcp_f32_e32 v100, v92
	v_cvt_f32_i32_e32 v92, v97
	v_mul_f32_e32 v97, v169, v111
	v_add_f32_e32 v96, 1.0, v96
	v_rcp_f32_e32 v96, v96
	v_fma_f32 v92, v97, v92, v115
	v_mul_f32_e32 v97, v169, v105
	v_fma_f32 v93, v97, v93, v101
	v_cvt_f32_i32_e32 v97, v98
	v_mul_f32_e32 v98, v169, v112
	v_mul_f32_e32 v92, 0xbfb8aa3b, v92
	v_exp_f32_e32 v92, v92
	v_fma_f32 v97, v98, v97, v116
	v_mul_f32_e32 v98, v169, v106
	v_fma_f32 v94, v98, v94, v102
	v_cvt_f32_i32_e32 v98, v99
	v_mul_f32_e32 v99, v169, v113
	v_mul_f32_e32 v97, 0xbfb8aa3b, v97
	v_exp_f32_e32 v97, v97
	v_fmac_f32_e32 v117, v99, v98
	v_mul_f32_e32 v98, 0xbfb8aa3b, v117
	v_exp_f32_e32 v98, v98
	v_mul_f32_e32 v93, 0xbfb8aa3b, v93
	v_mul_f32_e32 v99, v169, v107
	v_add_f32_e32 v92, 1.0, v92
	v_exp_f32_e32 v93, v93
	v_mul_f32_e32 v94, 0xbfb8aa3b, v94
	v_fmac_f32_e32 v103, v99, v95
	v_rcp_f32_e32 v92, v92
	v_add_f32_e32 v97, 1.0, v97
	v_exp_f32_e32 v94, v94
	v_mul_f32_e32 v95, 0xbfb8aa3b, v103
	v_rcp_f32_e32 v97, v97
	v_add_f32_e32 v98, 1.0, v98
	v_exp_f32_e32 v95, v95
	v_rcp_f32_e32 v98, v98
	v_add_f32_e32 v93, 1.0, v93
	v_mul_f32_e32 v96, 0x437f0000, v96
	v_rcp_f32_e32 v93, v93
	v_add_f32_e32 v94, 1.0, v94
	v_cvt_pk_u8_f32 v96, v96, 0, 0
	v_mul_f32_e32 v92, 0x437f0000, v92
	v_rcp_f32_e32 v94, v94
	v_add_f32_e32 v95, 1.0, v95
	v_cvt_pk_u8_f32 v92, v92, 1, v96
	v_mul_f32_e32 v96, 0x437f0000, v97
	v_rcp_f32_e32 v95, v95
	v_cvt_pk_u8_f32 v92, v96, 2, v92
	v_mul_f32_e32 v96, 0x437f0000, v98
	v_cvt_pk_u8_f32 v92, v96, 3, v92
	v_mul_f32_e32 v96, 0x437f0000, v100
	v_cvt_pk_u8_f32 v96, v96, 0, 0
	v_mul_f32_e32 v93, 0x437f0000, v93
	v_cvt_pk_u8_f32 v93, v93, 1, v96
	v_mul_f32_e32 v94, 0x437f0000, v94
	v_cvt_pk_u8_f32 v93, v94, 2, v93
	v_mul_f32_e32 v94, 0x437f0000, v95
	v_cvt_pk_u8_f32 v93, v94, 3, v93
	global_store_dwordx2 v[108:109], v[92:93], off
	v_mov_b64_e32 v[96:97], v[204:205]
	v_mov_b64_e32 v[98:99], v[206:207]
	v_mov_b64_e32 v[100:101], v[208:209]
	v_mov_b64_e32 v[102:103], v[210:211]
	s_nop 0
	v_mov_b64_e32 v[92:93], v[212:213]
	v_mov_b64_e32 v[94:95], v[214:215]
	v_mov_b64_e32 v[104:105], v[216:217]
	v_mov_b64_e32 v[106:107], v[218:219]
	v_mul_f32_e32 v96, v169, v96
	v_mul_f32_e32 v100, v169, v100
	v_fma_f32 v84, v96, v84, v92
	v_mul_f32_e32 v84, 0xbfb8aa3b, v84
	v_exp_f32_e32 v84, v84
	v_fma_f32 v88, v100, v88, v104
	v_mul_f32_e32 v88, 0xbfb8aa3b, v88
	v_exp_f32_e32 v88, v88
	v_add_f32_e32 v84, 1.0, v84
	v_rcp_f32_e32 v92, v84
	v_cvt_f32_i32_e32 v84, v89
	v_mul_f32_e32 v89, v169, v101
	v_add_f32_e32 v88, 1.0, v88
	v_rcp_f32_e32 v88, v88
	v_fma_f32 v84, v89, v84, v105
	v_mul_f32_e32 v89, v169, v97
	v_fma_f32 v85, v89, v85, v93
	v_cvt_f32_i32_e32 v89, v90
	v_mul_f32_e32 v90, v169, v102
	v_mul_f32_e32 v84, 0xbfb8aa3b, v84
	v_exp_f32_e32 v84, v84
	v_fma_f32 v89, v90, v89, v106
	v_mul_f32_e32 v90, v169, v98
	v_fma_f32 v86, v90, v86, v94
	v_cvt_f32_i32_e32 v90, v91
	v_mul_f32_e32 v91, v169, v103
	v_mul_f32_e32 v89, 0xbfb8aa3b, v89
	v_exp_f32_e32 v89, v89
	v_fmac_f32_e32 v107, v91, v90
	v_mul_f32_e32 v90, 0xbfb8aa3b, v107
	v_exp_f32_e32 v90, v90
	v_mul_f32_e32 v85, 0xbfb8aa3b, v85
	v_mul_f32_e32 v91, v169, v99
	v_add_f32_e32 v84, 1.0, v84
	v_exp_f32_e32 v85, v85
	v_mul_f32_e32 v86, 0xbfb8aa3b, v86
	v_fmac_f32_e32 v95, v91, v87
	v_rcp_f32_e32 v84, v84
	v_add_f32_e32 v89, 1.0, v89
	v_exp_f32_e32 v86, v86
	v_mul_f32_e32 v87, 0xbfb8aa3b, v95
	v_rcp_f32_e32 v89, v89
	v_add_f32_e32 v90, 1.0, v90
	v_exp_f32_e32 v87, v87
	v_rcp_f32_e32 v90, v90
	v_add_f32_e32 v85, 1.0, v85
	v_mul_f32_e32 v88, 0x437f0000, v88
	v_rcp_f32_e32 v85, v85
	v_add_f32_e32 v86, 1.0, v86
	v_cvt_pk_u8_f32 v88, v88, 0, 0
	v_mul_f32_e32 v84, 0x437f0000, v84
	v_rcp_f32_e32 v86, v86
	v_add_f32_e32 v87, 1.0, v87
	v_cvt_pk_u8_f32 v84, v84, 1, v88
	v_mul_f32_e32 v88, 0x437f0000, v89
	v_rcp_f32_e32 v87, v87
	v_cvt_pk_u8_f32 v84, v88, 2, v84
	v_mul_f32_e32 v88, 0x437f0000, v90
	v_cvt_pk_u8_f32 v84, v88, 3, v84
	v_mul_f32_e32 v88, 0x437f0000, v92
	v_cvt_pk_u8_f32 v88, v88, 0, 0
	v_mul_f32_e32 v85, 0x437f0000, v85
	v_cvt_pk_u8_f32 v85, v85, 1, v88
	v_mul_f32_e32 v86, 0x437f0000, v86
	v_cvt_pk_u8_f32 v85, v86, 2, v85
	v_mul_f32_e32 v86, 0x437f0000, v87
	v_cvt_pk_u8_f32 v85, v86, 3, v85
	global_store_dwordx2 v[108:109], v[84:85], off offset:128
	v_mad_i64_i32 v[84:85], s[22:23], v166, s24, v[156:157]
	v_lshl_add_u64 v[84:85], v[84:85], 0, s[20:21]
	v_lshl_add_u64 v[84:85], v[84:85], 0, s[12:13]
	v_lshl_add_u64 v[92:93], v[84:85], 0, v[150:151]
	v_mov_b64_e32 v[88:89], v[188:189]
	v_mov_b64_e32 v[90:91], v[190:191]
	v_mov_b64_e32 v[94:95], v[192:193]
	v_mov_b64_e32 v[96:97], v[194:195]
	v_mov_b64_e32 v[84:85], v[196:197]
	v_mov_b64_e32 v[86:87], v[198:199]
	v_mov_b64_e32 v[98:99], v[200:201]
	v_mov_b64_e32 v[100:101], v[202:203]
	v_mul_f32_e32 v88, v167, v88
	v_mul_f32_e32 v94, v167, v94
	v_fma_f32 v76, v88, v76, v84
	v_mul_f32_e32 v76, 0xbfb8aa3b, v76
	v_exp_f32_e32 v76, v76
	v_fma_f32 v80, v94, v80, v98
	v_mul_f32_e32 v80, 0xbfb8aa3b, v80
	v_exp_f32_e32 v80, v80
	v_add_f32_e32 v76, 1.0, v76
	v_rcp_f32_e32 v84, v76
	v_cvt_f32_i32_e32 v76, v81
	v_mul_f32_e32 v81, v167, v95
	v_add_f32_e32 v80, 1.0, v80
	v_rcp_f32_e32 v80, v80
	v_fma_f32 v76, v81, v76, v99
	v_mul_f32_e32 v81, v167, v89
	v_fma_f32 v77, v81, v77, v85
	v_cvt_f32_i32_e32 v81, v82
	v_mul_f32_e32 v82, v167, v96
	v_mul_f32_e32 v76, 0xbfb8aa3b, v76
	v_exp_f32_e32 v76, v76
	v_fma_f32 v81, v82, v81, v100
	v_mul_f32_e32 v82, v167, v90
	v_fma_f32 v78, v82, v78, v86
	v_cvt_f32_i32_e32 v82, v83
	v_mul_f32_e32 v83, v167, v97
	v_mul_f32_e32 v81, 0xbfb8aa3b, v81
	v_exp_f32_e32 v81, v81
	v_fmac_f32_e32 v101, v83, v82
	v_mul_f32_e32 v82, 0xbfb8aa3b, v101
	v_exp_f32_e32 v82, v82
	v_mul_f32_e32 v77, 0xbfb8aa3b, v77
	v_mul_f32_e32 v83, v167, v91
	v_add_f32_e32 v76, 1.0, v76
	v_exp_f32_e32 v77, v77
	v_mul_f32_e32 v78, 0xbfb8aa3b, v78
	v_fmac_f32_e32 v87, v83, v79
	v_rcp_f32_e32 v76, v76
	v_add_f32_e32 v81, 1.0, v81
	v_exp_f32_e32 v78, v78
	v_mul_f32_e32 v79, 0xbfb8aa3b, v87
	v_rcp_f32_e32 v81, v81
	v_add_f32_e32 v82, 1.0, v82
	v_exp_f32_e32 v79, v79
	v_rcp_f32_e32 v82, v82
	v_add_f32_e32 v77, 1.0, v77
	v_mul_f32_e32 v80, 0x437f0000, v80
	v_rcp_f32_e32 v77, v77
	v_add_f32_e32 v78, 1.0, v78
	v_cvt_pk_u8_f32 v80, v80, 0, 0
	v_mul_f32_e32 v76, 0x437f0000, v76
	v_rcp_f32_e32 v78, v78
	v_add_f32_e32 v79, 1.0, v79
	v_cvt_pk_u8_f32 v76, v76, 1, v80
	v_mul_f32_e32 v80, 0x437f0000, v81
	v_rcp_f32_e32 v79, v79
	v_cvt_pk_u8_f32 v76, v80, 2, v76
	v_mul_f32_e32 v80, 0x437f0000, v82
	v_cvt_pk_u8_f32 v76, v80, 3, v76
	v_mul_f32_e32 v80, 0x437f0000, v84
	v_cvt_pk_u8_f32 v80, v80, 0, 0
	v_mul_f32_e32 v77, 0x437f0000, v77
	v_cvt_pk_u8_f32 v77, v77, 1, v80
	v_mul_f32_e32 v78, 0x437f0000, v78
	v_cvt_pk_u8_f32 v77, v78, 2, v77
	v_mul_f32_e32 v78, 0x437f0000, v79
	v_cvt_pk_u8_f32 v77, v78, 3, v77
	global_store_dwordx2 v[92:93], v[76:77], off
	v_mov_b64_e32 v[80:81], v[204:205]
	v_mov_b64_e32 v[82:83], v[206:207]
	v_mov_b64_e32 v[84:85], v[208:209]
	v_mov_b64_e32 v[86:87], v[210:211]
	s_nop 0
	v_mov_b64_e32 v[76:77], v[212:213]
	v_mov_b64_e32 v[78:79], v[214:215]
	v_mov_b64_e32 v[88:89], v[216:217]
	v_mov_b64_e32 v[90:91], v[218:219]
	v_mul_f32_e32 v80, v167, v80
	v_mul_f32_e32 v84, v167, v84
	v_fma_f32 v68, v80, v68, v76
	v_mul_f32_e32 v68, 0xbfb8aa3b, v68
	v_exp_f32_e32 v68, v68
	v_fma_f32 v72, v84, v72, v88
	v_mul_f32_e32 v72, 0xbfb8aa3b, v72
	v_exp_f32_e32 v72, v72
	v_add_f32_e32 v68, 1.0, v68
	v_rcp_f32_e32 v76, v68
	v_cvt_f32_i32_e32 v68, v73
	v_mul_f32_e32 v73, v167, v85
	v_add_f32_e32 v72, 1.0, v72
	v_rcp_f32_e32 v72, v72
	v_fma_f32 v68, v73, v68, v89
	v_mul_f32_e32 v73, v167, v81
	v_fma_f32 v69, v73, v69, v77
	v_cvt_f32_i32_e32 v73, v74
	v_mul_f32_e32 v74, v167, v86
	v_mul_f32_e32 v68, 0xbfb8aa3b, v68
	v_exp_f32_e32 v68, v68
	v_fma_f32 v73, v74, v73, v90
	v_mul_f32_e32 v74, v167, v82
	v_fma_f32 v70, v74, v70, v78
	v_cvt_f32_i32_e32 v74, v75
	v_mul_f32_e32 v75, v167, v87
	v_mul_f32_e32 v73, 0xbfb8aa3b, v73
	v_exp_f32_e32 v73, v73
	v_fmac_f32_e32 v91, v75, v74
	v_mul_f32_e32 v74, 0xbfb8aa3b, v91
	v_exp_f32_e32 v74, v74
	v_mul_f32_e32 v69, 0xbfb8aa3b, v69
	v_mul_f32_e32 v75, v167, v83
	v_add_f32_e32 v68, 1.0, v68
	v_exp_f32_e32 v69, v69
	v_mul_f32_e32 v70, 0xbfb8aa3b, v70
	v_fmac_f32_e32 v79, v75, v71
	v_rcp_f32_e32 v68, v68
	v_add_f32_e32 v73, 1.0, v73
	v_exp_f32_e32 v70, v70
	v_mul_f32_e32 v71, 0xbfb8aa3b, v79
	v_rcp_f32_e32 v73, v73
	v_add_f32_e32 v74, 1.0, v74
	v_exp_f32_e32 v71, v71
	v_rcp_f32_e32 v74, v74
	v_add_f32_e32 v69, 1.0, v69
	v_mul_f32_e32 v72, 0x437f0000, v72
	v_rcp_f32_e32 v69, v69
	v_add_f32_e32 v70, 1.0, v70
	v_cvt_pk_u8_f32 v72, v72, 0, 0
	v_mul_f32_e32 v68, 0x437f0000, v68
	v_rcp_f32_e32 v70, v70
	v_add_f32_e32 v71, 1.0, v71
	v_cvt_pk_u8_f32 v68, v68, 1, v72
	v_mul_f32_e32 v72, 0x437f0000, v73
	v_rcp_f32_e32 v71, v71
	v_cvt_pk_u8_f32 v68, v72, 2, v68
	v_mul_f32_e32 v72, 0x437f0000, v74
	v_cvt_pk_u8_f32 v68, v72, 3, v68
	v_mul_f32_e32 v72, 0x437f0000, v76
	v_cvt_pk_u8_f32 v72, v72, 0, 0
	v_mul_f32_e32 v69, 0x437f0000, v69
	v_cvt_pk_u8_f32 v69, v69, 1, v72
	v_mul_f32_e32 v70, 0x437f0000, v70
	v_cvt_pk_u8_f32 v69, v70, 2, v69
	v_mul_f32_e32 v70, 0x437f0000, v71
	v_cvt_pk_u8_f32 v69, v70, 3, v69
	global_store_dwordx2 v[92:93], v[68:69], off offset:128
	v_mad_i64_i32 v[68:69], s[22:23], v164, s24, v[156:157]
	v_lshl_add_u64 v[68:69], v[68:69], 0, s[20:21]
	v_lshl_add_u64 v[68:69], v[68:69], 0, s[12:13]
	v_lshl_add_u64 v[76:77], v[68:69], 0, v[150:151]
	v_mov_b64_e32 v[72:73], v[188:189]
	v_mov_b64_e32 v[74:75], v[190:191]
	v_mov_b64_e32 v[78:79], v[192:193]
	v_mov_b64_e32 v[80:81], v[194:195]
	v_mov_b64_e32 v[68:69], v[196:197]
	v_mov_b64_e32 v[70:71], v[198:199]
	v_mov_b64_e32 v[82:83], v[200:201]
	v_mov_b64_e32 v[84:85], v[202:203]
	v_mul_f32_e32 v72, v165, v72
	v_mul_f32_e32 v78, v165, v78
	v_fma_f32 v60, v72, v60, v68
	v_mul_f32_e32 v60, 0xbfb8aa3b, v60
	v_exp_f32_e32 v60, v60
	v_fma_f32 v64, v78, v64, v82
	v_mul_f32_e32 v64, 0xbfb8aa3b, v64
	v_exp_f32_e32 v64, v64
	v_add_f32_e32 v60, 1.0, v60
	v_rcp_f32_e32 v68, v60
	v_cvt_f32_i32_e32 v60, v65
	v_mul_f32_e32 v65, v165, v79
	v_add_f32_e32 v64, 1.0, v64
	v_rcp_f32_e32 v64, v64
	v_fma_f32 v60, v65, v60, v83
	v_mul_f32_e32 v65, v165, v73
	v_fma_f32 v61, v65, v61, v69
	v_cvt_f32_i32_e32 v65, v66
	v_mul_f32_e32 v66, v165, v80
	v_mul_f32_e32 v60, 0xbfb8aa3b, v60
	v_exp_f32_e32 v60, v60
	v_fma_f32 v65, v66, v65, v84
	v_mul_f32_e32 v66, v165, v74
	v_fma_f32 v62, v66, v62, v70
	v_cvt_f32_i32_e32 v66, v67
	v_mul_f32_e32 v67, v165, v81
	v_mul_f32_e32 v65, 0xbfb8aa3b, v65
	v_exp_f32_e32 v65, v65
	v_fmac_f32_e32 v85, v67, v66
	v_mul_f32_e32 v66, 0xbfb8aa3b, v85
	v_exp_f32_e32 v66, v66
	v_mul_f32_e32 v61, 0xbfb8aa3b, v61
	v_mul_f32_e32 v67, v165, v75
	v_add_f32_e32 v60, 1.0, v60
	v_exp_f32_e32 v61, v61
	v_mul_f32_e32 v62, 0xbfb8aa3b, v62
	v_fmac_f32_e32 v71, v67, v63
	v_rcp_f32_e32 v60, v60
	v_add_f32_e32 v65, 1.0, v65
	v_exp_f32_e32 v62, v62
	v_mul_f32_e32 v63, 0xbfb8aa3b, v71
	v_rcp_f32_e32 v65, v65
	v_add_f32_e32 v66, 1.0, v66
	v_exp_f32_e32 v63, v63
	v_rcp_f32_e32 v66, v66
	v_add_f32_e32 v61, 1.0, v61
	v_mul_f32_e32 v64, 0x437f0000, v64
	v_rcp_f32_e32 v61, v61
	v_add_f32_e32 v62, 1.0, v62
	v_cvt_pk_u8_f32 v64, v64, 0, 0
	v_mul_f32_e32 v60, 0x437f0000, v60
	v_rcp_f32_e32 v62, v62
	v_add_f32_e32 v63, 1.0, v63
	v_cvt_pk_u8_f32 v60, v60, 1, v64
	v_mul_f32_e32 v64, 0x437f0000, v65
	v_rcp_f32_e32 v63, v63
	v_cvt_pk_u8_f32 v60, v64, 2, v60
	v_mul_f32_e32 v64, 0x437f0000, v66
	v_cvt_pk_u8_f32 v60, v64, 3, v60
	v_mul_f32_e32 v64, 0x437f0000, v68
	v_cvt_pk_u8_f32 v64, v64, 0, 0
	v_mul_f32_e32 v61, 0x437f0000, v61
	v_cvt_pk_u8_f32 v61, v61, 1, v64
	v_mul_f32_e32 v62, 0x437f0000, v62
	v_cvt_pk_u8_f32 v61, v62, 2, v61
	v_mul_f32_e32 v62, 0x437f0000, v63
	v_cvt_pk_u8_f32 v61, v62, 3, v61
	global_store_dwordx2 v[76:77], v[60:61], off
	v_mov_b64_e32 v[64:65], v[204:205]
	v_mov_b64_e32 v[66:67], v[206:207]
	v_mov_b64_e32 v[68:69], v[208:209]
	v_mov_b64_e32 v[70:71], v[210:211]
	s_nop 0
	v_mov_b64_e32 v[60:61], v[212:213]
	v_mov_b64_e32 v[62:63], v[214:215]
	v_mov_b64_e32 v[72:73], v[216:217]
	v_mov_b64_e32 v[74:75], v[218:219]
	v_mul_f32_e32 v64, v165, v64
	v_mul_f32_e32 v68, v165, v68
	v_fma_f32 v52, v64, v52, v60
	v_mul_f32_e32 v52, 0xbfb8aa3b, v52
	v_exp_f32_e32 v52, v52
	v_fma_f32 v56, v68, v56, v72
	v_mul_f32_e32 v56, 0xbfb8aa3b, v56
	v_exp_f32_e32 v56, v56
	v_add_f32_e32 v52, 1.0, v52
	v_rcp_f32_e32 v60, v52
	v_cvt_f32_i32_e32 v52, v57
	v_mul_f32_e32 v57, v165, v69
	v_add_f32_e32 v56, 1.0, v56
	v_rcp_f32_e32 v56, v56
	v_fma_f32 v52, v57, v52, v73
	v_mul_f32_e32 v57, v165, v65
	v_fma_f32 v53, v57, v53, v61
	v_cvt_f32_i32_e32 v57, v58
	v_mul_f32_e32 v58, v165, v70
	v_mul_f32_e32 v52, 0xbfb8aa3b, v52
	v_exp_f32_e32 v52, v52
	v_fma_f32 v57, v58, v57, v74
	v_mul_f32_e32 v58, v165, v66
	v_fma_f32 v54, v58, v54, v62
	v_cvt_f32_i32_e32 v58, v59
	v_mul_f32_e32 v59, v165, v71
	v_mul_f32_e32 v57, 0xbfb8aa3b, v57
	v_exp_f32_e32 v57, v57
	v_fmac_f32_e32 v75, v59, v58
	v_mul_f32_e32 v58, 0xbfb8aa3b, v75
	v_exp_f32_e32 v58, v58
	v_mul_f32_e32 v53, 0xbfb8aa3b, v53
	v_mul_f32_e32 v59, v165, v67
	v_add_f32_e32 v52, 1.0, v52
	v_exp_f32_e32 v53, v53
	v_mul_f32_e32 v54, 0xbfb8aa3b, v54
	v_fmac_f32_e32 v63, v59, v55
	v_rcp_f32_e32 v52, v52
	v_add_f32_e32 v57, 1.0, v57
	v_exp_f32_e32 v54, v54
	v_mul_f32_e32 v55, 0xbfb8aa3b, v63
	v_rcp_f32_e32 v57, v57
	v_add_f32_e32 v58, 1.0, v58
	v_exp_f32_e32 v55, v55
	v_rcp_f32_e32 v58, v58
	v_add_f32_e32 v53, 1.0, v53
	v_mul_f32_e32 v56, 0x437f0000, v56
	v_rcp_f32_e32 v53, v53
	v_add_f32_e32 v54, 1.0, v54
	v_cvt_pk_u8_f32 v56, v56, 0, 0
	v_mul_f32_e32 v52, 0x437f0000, v52
	v_rcp_f32_e32 v54, v54
	v_add_f32_e32 v55, 1.0, v55
	v_cvt_pk_u8_f32 v52, v52, 1, v56
	v_mul_f32_e32 v56, 0x437f0000, v57
	v_rcp_f32_e32 v55, v55
	v_cvt_pk_u8_f32 v52, v56, 2, v52
	v_mul_f32_e32 v56, 0x437f0000, v58
	v_cvt_pk_u8_f32 v52, v56, 3, v52
	v_mul_f32_e32 v56, 0x437f0000, v60
	v_cvt_pk_u8_f32 v56, v56, 0, 0
	v_mul_f32_e32 v53, 0x437f0000, v53
	v_cvt_pk_u8_f32 v53, v53, 1, v56
	v_mul_f32_e32 v54, 0x437f0000, v54
	v_cvt_pk_u8_f32 v53, v54, 2, v53
	v_mul_f32_e32 v54, 0x437f0000, v55
	v_cvt_pk_u8_f32 v53, v54, 3, v53
	global_store_dwordx2 v[76:77], v[52:53], off offset:128
	v_mad_i64_i32 v[52:53], s[22:23], v162, s24, v[156:157]
	v_lshl_add_u64 v[52:53], v[52:53], 0, s[20:21]
	v_lshl_add_u64 v[52:53], v[52:53], 0, s[12:13]
	v_lshl_add_u64 v[60:61], v[52:53], 0, v[150:151]
	v_mov_b64_e32 v[56:57], v[188:189]
	v_mov_b64_e32 v[58:59], v[190:191]
	v_mov_b64_e32 v[62:63], v[192:193]
	v_mov_b64_e32 v[64:65], v[194:195]
	v_mov_b64_e32 v[52:53], v[196:197]
	v_mov_b64_e32 v[54:55], v[198:199]
	v_mov_b64_e32 v[66:67], v[200:201]
	v_mov_b64_e32 v[68:69], v[202:203]
	v_mul_f32_e32 v56, v163, v56
	v_mul_f32_e32 v62, v163, v62
	v_fma_f32 v44, v56, v44, v52
	v_mul_f32_e32 v44, 0xbfb8aa3b, v44
	v_exp_f32_e32 v44, v44
	v_fma_f32 v48, v62, v48, v66
	v_mul_f32_e32 v48, 0xbfb8aa3b, v48
	v_exp_f32_e32 v48, v48
	v_add_f32_e32 v44, 1.0, v44
	v_rcp_f32_e32 v52, v44
	v_cvt_f32_i32_e32 v44, v49
	v_mul_f32_e32 v49, v163, v63
	v_add_f32_e32 v48, 1.0, v48
	v_rcp_f32_e32 v48, v48
	v_fma_f32 v44, v49, v44, v67
	v_mul_f32_e32 v49, v163, v57
	v_fma_f32 v45, v49, v45, v53
	v_cvt_f32_i32_e32 v49, v50
	v_mul_f32_e32 v50, v163, v64
	v_mul_f32_e32 v44, 0xbfb8aa3b, v44
	v_exp_f32_e32 v44, v44
	v_fma_f32 v49, v50, v49, v68
	v_mul_f32_e32 v50, v163, v58
	v_fma_f32 v46, v50, v46, v54
	v_cvt_f32_i32_e32 v50, v51
	v_mul_f32_e32 v51, v163, v65
	v_mul_f32_e32 v49, 0xbfb8aa3b, v49
	v_exp_f32_e32 v49, v49
	v_fmac_f32_e32 v69, v51, v50
	v_mul_f32_e32 v50, 0xbfb8aa3b, v69
	v_exp_f32_e32 v50, v50
	v_mul_f32_e32 v45, 0xbfb8aa3b, v45
	v_mul_f32_e32 v51, v163, v59
	v_add_f32_e32 v44, 1.0, v44
	v_exp_f32_e32 v45, v45
	v_mul_f32_e32 v46, 0xbfb8aa3b, v46
	v_fmac_f32_e32 v55, v51, v47
	v_rcp_f32_e32 v44, v44
	v_add_f32_e32 v49, 1.0, v49
	v_exp_f32_e32 v46, v46
	v_mul_f32_e32 v47, 0xbfb8aa3b, v55
	v_rcp_f32_e32 v49, v49
	v_add_f32_e32 v50, 1.0, v50
	v_exp_f32_e32 v47, v47
	v_rcp_f32_e32 v50, v50
	v_add_f32_e32 v45, 1.0, v45
	v_mul_f32_e32 v48, 0x437f0000, v48
	v_rcp_f32_e32 v45, v45
	v_add_f32_e32 v46, 1.0, v46
	v_cvt_pk_u8_f32 v48, v48, 0, 0
	v_mul_f32_e32 v44, 0x437f0000, v44
	v_rcp_f32_e32 v46, v46
	v_add_f32_e32 v47, 1.0, v47
	v_cvt_pk_u8_f32 v44, v44, 1, v48
	v_mul_f32_e32 v48, 0x437f0000, v49
	v_rcp_f32_e32 v47, v47
	v_cvt_pk_u8_f32 v44, v48, 2, v44
	v_mul_f32_e32 v48, 0x437f0000, v50
	v_cvt_pk_u8_f32 v44, v48, 3, v44
	v_mul_f32_e32 v48, 0x437f0000, v52
	v_cvt_pk_u8_f32 v48, v48, 0, 0
	v_mul_f32_e32 v45, 0x437f0000, v45
	v_cvt_pk_u8_f32 v45, v45, 1, v48
	v_mul_f32_e32 v46, 0x437f0000, v46
	v_cvt_pk_u8_f32 v45, v46, 2, v45
	v_mul_f32_e32 v46, 0x437f0000, v47
	v_cvt_pk_u8_f32 v45, v46, 3, v45
	global_store_dwordx2 v[60:61], v[44:45], off
	v_mov_b64_e32 v[48:49], v[204:205]
	v_mov_b64_e32 v[50:51], v[206:207]
	v_mov_b64_e32 v[52:53], v[208:209]
	v_mov_b64_e32 v[54:55], v[210:211]
	s_nop 0
	v_mov_b64_e32 v[44:45], v[212:213]
	v_mov_b64_e32 v[46:47], v[214:215]
	v_mov_b64_e32 v[56:57], v[216:217]
	v_mov_b64_e32 v[58:59], v[218:219]
	v_mul_f32_e32 v48, v163, v48
	v_mul_f32_e32 v52, v163, v52
	v_fma_f32 v36, v48, v36, v44
	v_mul_f32_e32 v36, 0xbfb8aa3b, v36
	v_exp_f32_e32 v36, v36
	v_fma_f32 v40, v52, v40, v56
	v_mul_f32_e32 v40, 0xbfb8aa3b, v40
	v_exp_f32_e32 v40, v40
	v_add_f32_e32 v36, 1.0, v36
	v_rcp_f32_e32 v44, v36
	v_cvt_f32_i32_e32 v36, v41
	v_mul_f32_e32 v41, v163, v53
	v_add_f32_e32 v40, 1.0, v40
	v_rcp_f32_e32 v40, v40
	v_fma_f32 v36, v41, v36, v57
	v_mul_f32_e32 v41, v163, v49
	v_fma_f32 v37, v41, v37, v45
	v_cvt_f32_i32_e32 v41, v42
	v_mul_f32_e32 v42, v163, v54
	v_mul_f32_e32 v36, 0xbfb8aa3b, v36
	v_exp_f32_e32 v36, v36
	v_fma_f32 v41, v42, v41, v58
	v_mul_f32_e32 v42, v163, v50
	v_fma_f32 v38, v42, v38, v46
	v_cvt_f32_i32_e32 v42, v43
	v_mul_f32_e32 v43, v163, v55
	v_mul_f32_e32 v41, 0xbfb8aa3b, v41
	v_exp_f32_e32 v41, v41
	v_fmac_f32_e32 v59, v43, v42
	v_mul_f32_e32 v42, 0xbfb8aa3b, v59
	v_exp_f32_e32 v42, v42
	v_mul_f32_e32 v37, 0xbfb8aa3b, v37
	v_mul_f32_e32 v43, v163, v51
	v_add_f32_e32 v36, 1.0, v36
	v_exp_f32_e32 v37, v37
	v_mul_f32_e32 v38, 0xbfb8aa3b, v38
	v_fmac_f32_e32 v47, v43, v39
	v_rcp_f32_e32 v36, v36
	v_add_f32_e32 v41, 1.0, v41
	v_exp_f32_e32 v38, v38
	v_mul_f32_e32 v39, 0xbfb8aa3b, v47
	v_rcp_f32_e32 v41, v41
	v_add_f32_e32 v42, 1.0, v42
	v_exp_f32_e32 v39, v39
	v_rcp_f32_e32 v42, v42
	v_add_f32_e32 v37, 1.0, v37
	v_mul_f32_e32 v40, 0x437f0000, v40
	v_rcp_f32_e32 v37, v37
	v_add_f32_e32 v38, 1.0, v38
	v_cvt_pk_u8_f32 v40, v40, 0, 0
	v_mul_f32_e32 v36, 0x437f0000, v36
	v_rcp_f32_e32 v38, v38
	v_add_f32_e32 v39, 1.0, v39
	v_cvt_pk_u8_f32 v36, v36, 1, v40
	v_mul_f32_e32 v40, 0x437f0000, v41
	v_rcp_f32_e32 v39, v39
	v_cvt_pk_u8_f32 v36, v40, 2, v36
	v_mul_f32_e32 v40, 0x437f0000, v42
	v_cvt_pk_u8_f32 v36, v40, 3, v36
	v_mul_f32_e32 v40, 0x437f0000, v44
	v_cvt_pk_u8_f32 v40, v40, 0, 0
	v_mul_f32_e32 v37, 0x437f0000, v37
	v_cvt_pk_u8_f32 v37, v37, 1, v40
	v_mul_f32_e32 v38, 0x437f0000, v38
	v_cvt_pk_u8_f32 v37, v38, 2, v37
	v_mul_f32_e32 v38, 0x437f0000, v39
	v_cvt_pk_u8_f32 v37, v38, 3, v37
	global_store_dwordx2 v[60:61], v[36:37], off offset:128
	v_mad_i64_i32 v[36:37], s[22:23], v160, s24, v[156:157]
	v_lshl_add_u64 v[36:37], v[36:37], 0, s[20:21]
	v_lshl_add_u64 v[36:37], v[36:37], 0, s[12:13]
	v_lshl_add_u64 v[44:45], v[36:37], 0, v[150:151]
	v_mov_b64_e32 v[40:41], v[188:189]
	v_mov_b64_e32 v[42:43], v[190:191]
	v_mov_b64_e32 v[46:47], v[192:193]
	v_mov_b64_e32 v[48:49], v[194:195]
	v_mov_b64_e32 v[36:37], v[196:197]
	v_mov_b64_e32 v[38:39], v[198:199]
	v_mov_b64_e32 v[50:51], v[200:201]
	v_mov_b64_e32 v[52:53], v[202:203]
	v_mul_f32_e32 v40, v161, v40
	v_mul_f32_e32 v46, v161, v46
	v_fma_f32 v28, v40, v28, v36
	v_mul_f32_e32 v28, 0xbfb8aa3b, v28
	v_exp_f32_e32 v28, v28
	v_fma_f32 v32, v46, v32, v50
	v_mul_f32_e32 v32, 0xbfb8aa3b, v32
	v_exp_f32_e32 v32, v32
	v_add_f32_e32 v28, 1.0, v28
	v_rcp_f32_e32 v36, v28
	v_cvt_f32_i32_e32 v28, v33
	v_mul_f32_e32 v33, v161, v47
	v_add_f32_e32 v32, 1.0, v32
	v_rcp_f32_e32 v32, v32
	v_fma_f32 v28, v33, v28, v51
	v_mul_f32_e32 v33, v161, v41
	v_fma_f32 v29, v33, v29, v37
	v_cvt_f32_i32_e32 v33, v34
	v_mul_f32_e32 v34, v161, v48
	v_mul_f32_e32 v28, 0xbfb8aa3b, v28
	v_exp_f32_e32 v28, v28
	v_fma_f32 v33, v34, v33, v52
	v_mul_f32_e32 v34, v161, v42
	v_fma_f32 v30, v34, v30, v38
	v_cvt_f32_i32_e32 v34, v35
	v_mul_f32_e32 v35, v161, v49
	v_mul_f32_e32 v33, 0xbfb8aa3b, v33
	v_exp_f32_e32 v33, v33
	v_fmac_f32_e32 v53, v35, v34
	v_mul_f32_e32 v34, 0xbfb8aa3b, v53
	v_exp_f32_e32 v34, v34
	v_mul_f32_e32 v29, 0xbfb8aa3b, v29
	v_mul_f32_e32 v35, v161, v43
	v_add_f32_e32 v28, 1.0, v28
	v_exp_f32_e32 v29, v29
	v_mul_f32_e32 v30, 0xbfb8aa3b, v30
	v_fmac_f32_e32 v39, v35, v31
	v_rcp_f32_e32 v28, v28
	v_add_f32_e32 v33, 1.0, v33
	v_exp_f32_e32 v30, v30
	v_mul_f32_e32 v31, 0xbfb8aa3b, v39
	v_rcp_f32_e32 v33, v33
	v_add_f32_e32 v34, 1.0, v34
	v_exp_f32_e32 v31, v31
	v_rcp_f32_e32 v34, v34
	v_add_f32_e32 v29, 1.0, v29
	v_mul_f32_e32 v32, 0x437f0000, v32
	v_rcp_f32_e32 v29, v29
	v_add_f32_e32 v30, 1.0, v30
	v_cvt_pk_u8_f32 v32, v32, 0, 0
	v_mul_f32_e32 v28, 0x437f0000, v28
	v_rcp_f32_e32 v30, v30
	v_add_f32_e32 v31, 1.0, v31
	v_cvt_pk_u8_f32 v28, v28, 1, v32
	v_mul_f32_e32 v32, 0x437f0000, v33
	v_rcp_f32_e32 v31, v31
	v_cvt_pk_u8_f32 v28, v32, 2, v28
	v_mul_f32_e32 v32, 0x437f0000, v34
	v_cvt_pk_u8_f32 v28, v32, 3, v28
	v_mul_f32_e32 v32, 0x437f0000, v36
	v_cvt_pk_u8_f32 v32, v32, 0, 0
	v_mul_f32_e32 v29, 0x437f0000, v29
	v_cvt_pk_u8_f32 v29, v29, 1, v32
	v_mul_f32_e32 v30, 0x437f0000, v30
	v_cvt_pk_u8_f32 v29, v30, 2, v29
	v_mul_f32_e32 v30, 0x437f0000, v31
	v_cvt_pk_u8_f32 v29, v30, 3, v29
	global_store_dwordx2 v[44:45], v[28:29], off
	v_mov_b64_e32 v[32:33], v[204:205]
	v_mov_b64_e32 v[34:35], v[206:207]
	v_mov_b64_e32 v[36:37], v[208:209]
	v_mov_b64_e32 v[38:39], v[210:211]
	s_nop 0
	v_mov_b64_e32 v[28:29], v[212:213]
	v_mov_b64_e32 v[30:31], v[214:215]
	v_mov_b64_e32 v[40:41], v[216:217]
	v_mov_b64_e32 v[42:43], v[218:219]
	v_mul_f32_e32 v32, v161, v32
	v_mul_f32_e32 v36, v161, v36
	v_fma_f32 v20, v32, v20, v28
	v_mul_f32_e32 v20, 0xbfb8aa3b, v20
	v_exp_f32_e32 v20, v20
	v_fma_f32 v24, v36, v24, v40
	v_mul_f32_e32 v24, 0xbfb8aa3b, v24
	v_exp_f32_e32 v24, v24
	v_add_f32_e32 v20, 1.0, v20
	v_rcp_f32_e32 v28, v20
	v_cvt_f32_i32_e32 v20, v25
	v_mul_f32_e32 v25, v161, v37
	v_add_f32_e32 v24, 1.0, v24
	v_rcp_f32_e32 v24, v24
	v_fma_f32 v20, v25, v20, v41
	v_mul_f32_e32 v25, v161, v33
	v_fma_f32 v21, v25, v21, v29
	v_cvt_f32_i32_e32 v25, v26
	v_mul_f32_e32 v26, v161, v38
	v_mul_f32_e32 v20, 0xbfb8aa3b, v20
	v_exp_f32_e32 v20, v20
	v_fma_f32 v25, v26, v25, v42
	v_mul_f32_e32 v26, v161, v34
	v_fma_f32 v22, v26, v22, v30
	v_cvt_f32_i32_e32 v26, v27
	v_mul_f32_e32 v27, v161, v39
	v_mul_f32_e32 v25, 0xbfb8aa3b, v25
	v_exp_f32_e32 v25, v25
	v_fmac_f32_e32 v43, v27, v26
	v_mul_f32_e32 v26, 0xbfb8aa3b, v43
	v_exp_f32_e32 v26, v26
	v_mul_f32_e32 v21, 0xbfb8aa3b, v21
	v_mul_f32_e32 v27, v161, v35
	v_add_f32_e32 v20, 1.0, v20
	v_exp_f32_e32 v21, v21
	v_mul_f32_e32 v22, 0xbfb8aa3b, v22
	v_fmac_f32_e32 v31, v27, v23
	v_rcp_f32_e32 v20, v20
	v_add_f32_e32 v25, 1.0, v25
	v_exp_f32_e32 v22, v22
	v_mul_f32_e32 v23, 0xbfb8aa3b, v31
	v_rcp_f32_e32 v25, v25
	v_add_f32_e32 v26, 1.0, v26
	v_exp_f32_e32 v23, v23
	v_rcp_f32_e32 v26, v26
	v_add_f32_e32 v21, 1.0, v21
	v_mul_f32_e32 v24, 0x437f0000, v24
	v_rcp_f32_e32 v21, v21
	v_add_f32_e32 v22, 1.0, v22
	v_cvt_pk_u8_f32 v24, v24, 0, 0
	v_mul_f32_e32 v20, 0x437f0000, v20
	v_rcp_f32_e32 v22, v22
	v_add_f32_e32 v23, 1.0, v23
	v_cvt_pk_u8_f32 v20, v20, 1, v24
	v_mul_f32_e32 v24, 0x437f0000, v25
	v_rcp_f32_e32 v23, v23
	v_cvt_pk_u8_f32 v20, v24, 2, v20
	v_mul_f32_e32 v24, 0x437f0000, v26
	v_cvt_pk_u8_f32 v20, v24, 3, v20
	v_mul_f32_e32 v24, 0x437f0000, v28
	v_cvt_pk_u8_f32 v24, v24, 0, 0
	v_mul_f32_e32 v21, 0x437f0000, v21
	v_cvt_pk_u8_f32 v21, v21, 1, v24
	v_mul_f32_e32 v22, 0x437f0000, v22
	v_cvt_pk_u8_f32 v21, v22, 2, v21
	v_mul_f32_e32 v22, 0x437f0000, v23
	v_cvt_pk_u8_f32 v21, v22, 3, v21
	global_store_dwordx2 v[44:45], v[20:21], off offset:128
	v_mad_i64_i32 v[20:21], s[22:23], v154, s24, v[156:157]
	v_lshl_add_u64 v[20:21], v[20:21], 0, s[20:21]
	v_lshl_add_u64 v[20:21], v[20:21], 0, s[12:13]
	v_lshl_add_u64 v[28:29], v[20:21], 0, v[150:151]
	v_mov_b64_e32 v[24:25], v[188:189]
	v_mov_b64_e32 v[26:27], v[190:191]
	v_mov_b64_e32 v[30:31], v[192:193]
	v_mov_b64_e32 v[32:33], v[194:195]
	v_mov_b64_e32 v[20:21], v[196:197]
	v_mov_b64_e32 v[22:23], v[198:199]
	v_mov_b64_e32 v[34:35], v[200:201]
	v_mov_b64_e32 v[36:37], v[202:203]
	s_mov_b64 s[20:21], -1
	v_mul_f32_e32 v24, v155, v24
	v_mul_f32_e32 v30, v155, v30
	v_fma_f32 v12, v24, v12, v20
	v_mul_f32_e32 v12, 0xbfb8aa3b, v12
	v_exp_f32_e32 v12, v12
	v_fma_f32 v16, v30, v16, v34
	v_mul_f32_e32 v16, 0xbfb8aa3b, v16
	v_exp_f32_e32 v16, v16
	v_add_f32_e32 v12, 1.0, v12
	v_rcp_f32_e32 v20, v12
	v_cvt_f32_i32_e32 v12, v17
	v_mul_f32_e32 v17, v155, v31
	v_add_f32_e32 v16, 1.0, v16
	v_rcp_f32_e32 v16, v16
	v_fma_f32 v12, v17, v12, v35
	v_mul_f32_e32 v17, v155, v25
	v_fma_f32 v13, v17, v13, v21
	v_cvt_f32_i32_e32 v17, v18
	v_mul_f32_e32 v18, v155, v32
	v_mul_f32_e32 v12, 0xbfb8aa3b, v12
	v_exp_f32_e32 v12, v12
	v_fma_f32 v17, v18, v17, v36
	v_mul_f32_e32 v18, v155, v26
	v_fma_f32 v14, v18, v14, v22
	v_cvt_f32_i32_e32 v18, v19
	v_mul_f32_e32 v19, v155, v33
	v_mul_f32_e32 v17, 0xbfb8aa3b, v17
	v_exp_f32_e32 v17, v17
	v_fmac_f32_e32 v37, v19, v18
	v_mul_f32_e32 v18, 0xbfb8aa3b, v37
	v_exp_f32_e32 v18, v18
	v_mul_f32_e32 v13, 0xbfb8aa3b, v13
	v_mul_f32_e32 v19, v155, v27
	v_add_f32_e32 v12, 1.0, v12
	v_exp_f32_e32 v13, v13
	v_mul_f32_e32 v14, 0xbfb8aa3b, v14
	v_fmac_f32_e32 v23, v19, v15
	v_rcp_f32_e32 v12, v12
	v_add_f32_e32 v17, 1.0, v17
	v_exp_f32_e32 v14, v14
	v_mul_f32_e32 v15, 0xbfb8aa3b, v23
	v_rcp_f32_e32 v17, v17
	v_add_f32_e32 v18, 1.0, v18
	v_exp_f32_e32 v15, v15
	v_rcp_f32_e32 v18, v18
	v_add_f32_e32 v13, 1.0, v13
	v_mul_f32_e32 v16, 0x437f0000, v16
	v_rcp_f32_e32 v13, v13
	v_add_f32_e32 v14, 1.0, v14
	v_cvt_pk_u8_f32 v16, v16, 0, 0
	v_mul_f32_e32 v12, 0x437f0000, v12
	v_rcp_f32_e32 v14, v14
	v_add_f32_e32 v15, 1.0, v15
	v_cvt_pk_u8_f32 v12, v12, 1, v16
	v_mul_f32_e32 v16, 0x437f0000, v17
	v_rcp_f32_e32 v15, v15
	v_cvt_pk_u8_f32 v12, v16, 2, v12
	v_mul_f32_e32 v16, 0x437f0000, v18
	v_cvt_pk_u8_f32 v12, v16, 3, v12
	v_mul_f32_e32 v16, 0x437f0000, v20
	v_cvt_pk_u8_f32 v16, v16, 0, 0
	v_mul_f32_e32 v13, 0x437f0000, v13
	v_cvt_pk_u8_f32 v13, v13, 1, v16
	v_mul_f32_e32 v14, 0x437f0000, v14
	v_cvt_pk_u8_f32 v13, v14, 2, v13
	v_mul_f32_e32 v14, 0x437f0000, v15
	v_cvt_pk_u8_f32 v13, v14, 3, v13
	global_store_dwordx2 v[28:29], v[12:13], off
	v_mov_b64_e32 v[16:17], v[204:205]
	v_mov_b64_e32 v[18:19], v[206:207]
	v_mov_b64_e32 v[20:21], v[208:209]
	v_mov_b64_e32 v[22:23], v[210:211]
	s_nop 0
	v_mov_b64_e32 v[12:13], v[212:213]
	v_mov_b64_e32 v[14:15], v[214:215]
	v_mov_b64_e32 v[24:25], v[216:217]
	v_mov_b64_e32 v[26:27], v[218:219]
	v_mul_f32_e32 v16, v155, v16
	v_mul_f32_e32 v20, v155, v20
	v_fma_f32 v4, v16, v4, v12
	v_mul_f32_e32 v4, 0xbfb8aa3b, v4
	v_exp_f32_e32 v4, v4
	v_fma_f32 v8, v20, v8, v24
	v_mul_f32_e32 v8, 0xbfb8aa3b, v8
	v_exp_f32_e32 v8, v8
	v_add_f32_e32 v4, 1.0, v4
	v_rcp_f32_e32 v12, v4
	v_cvt_f32_i32_e32 v4, v9
	v_mul_f32_e32 v9, v155, v21
	v_add_f32_e32 v8, 1.0, v8
	v_rcp_f32_e32 v8, v8
	v_fma_f32 v4, v9, v4, v25
	v_mul_f32_e32 v9, v155, v17
	v_fma_f32 v5, v9, v5, v13
	v_cvt_f32_i32_e32 v9, v10
	v_mul_f32_e32 v10, v155, v22
	v_mul_f32_e32 v4, 0xbfb8aa3b, v4
	v_exp_f32_e32 v4, v4
	v_fma_f32 v9, v10, v9, v26
	v_mul_f32_e32 v10, v155, v18
	v_fma_f32 v6, v10, v6, v14
	v_cvt_f32_i32_e32 v10, v11
	v_mul_f32_e32 v11, v155, v23
	v_mul_f32_e32 v9, 0xbfb8aa3b, v9
	v_exp_f32_e32 v9, v9
	v_fmac_f32_e32 v27, v11, v10
	v_mul_f32_e32 v10, 0xbfb8aa3b, v27
	v_exp_f32_e32 v10, v10
	v_mul_f32_e32 v5, 0xbfb8aa3b, v5
	v_mul_f32_e32 v11, v155, v19
	v_add_f32_e32 v4, 1.0, v4
	v_exp_f32_e32 v5, v5
	v_mul_f32_e32 v6, 0xbfb8aa3b, v6
	v_fmac_f32_e32 v15, v11, v7
	v_rcp_f32_e32 v4, v4
	v_add_f32_e32 v9, 1.0, v9
	v_exp_f32_e32 v6, v6
	v_mul_f32_e32 v7, 0xbfb8aa3b, v15
	v_rcp_f32_e32 v9, v9
	v_add_f32_e32 v10, 1.0, v10
	v_exp_f32_e32 v7, v7
	v_rcp_f32_e32 v10, v10
	v_add_f32_e32 v5, 1.0, v5
	v_mul_f32_e32 v8, 0x437f0000, v8
	v_rcp_f32_e32 v5, v5
	v_add_f32_e32 v6, 1.0, v6
	v_cvt_pk_u8_f32 v8, v8, 0, 0
	v_mul_f32_e32 v4, 0x437f0000, v4
	v_rcp_f32_e32 v6, v6
	v_add_f32_e32 v7, 1.0, v7
	v_cvt_pk_u8_f32 v4, v4, 1, v8
	v_mul_f32_e32 v8, 0x437f0000, v9
	v_rcp_f32_e32 v7, v7
	v_cvt_pk_u8_f32 v4, v8, 2, v4
	v_mul_f32_e32 v8, 0x437f0000, v10
	v_cvt_pk_u8_f32 v4, v8, 3, v4
	v_mul_f32_e32 v8, 0x437f0000, v12
	v_cvt_pk_u8_f32 v8, v8, 0, 0
	v_mul_f32_e32 v5, 0x437f0000, v5
	v_cvt_pk_u8_f32 v5, v5, 1, v8
	v_mul_f32_e32 v6, 0x437f0000, v6
	v_cvt_pk_u8_f32 v5, v6, 2, v5
	v_mul_f32_e32 v6, 0x437f0000, v7
	v_cvt_pk_u8_f32 v5, v6, 3, v5
	global_store_dwordx2 v[28:29], v[4:5], off offset:128
	s_cbranch_vccnz .LBB0_969
	s_andn2_b64 vcc, exec, s[0:1]
	s_cbranch_vccnz .LBB0_968
	s_barrier
	s_branch .LBB0_968

.LBB0_1490:
	s_mov_b64 s[16:17], 0
	s_movk_i32 s23, 0x5680
	v_mad_i64_i32 v[132:133], s[14:15], v10, s23, v[6:7]
	v_mov_b32_e32 v17, 0
	v_mov_b32_e32 v18, 0
	s_mov_b32 s24, 0x5680
	s_mov_b32 s25, 0
	s_mov_b32 s19, 8
.Lp1b_max:
	global_load_dword v116, v[132:133], off
	v_lshl_add_u64 v[132:133], v[132:133], 0, s[24:25]
	global_load_dword v117, v[132:133], off
	v_lshl_add_u64 v[132:133], v[132:133], 0, s[24:25]
	global_load_dword v118, v[132:133], off
	v_lshl_add_u64 v[132:133], v[132:133], 0, s[24:25]
	global_load_dword v119, v[132:133], off
	v_lshl_add_u64 v[132:133], v[132:133], 0, s[24:25]
	global_load_dword v120, v[132:133], off
	v_lshl_add_u64 v[132:133], v[132:133], 0, s[24:25]
	global_load_dword v121, v[132:133], off
	v_lshl_add_u64 v[132:133], v[132:133], 0, s[24:25]
	global_load_dword v122, v[132:133], off
	v_lshl_add_u64 v[132:133], v[132:133], 0, s[24:25]
	global_load_dword v123, v[132:133], off
	v_lshl_add_u64 v[132:133], v[132:133], 0, s[24:25]
	global_load_dword v124, v[132:133], off
	v_lshl_add_u64 v[132:133], v[132:133], 0, s[24:25]
	global_load_dword v125, v[132:133], off
	v_lshl_add_u64 v[132:133], v[132:133], 0, s[24:25]
	global_load_dword v126, v[132:133], off
	v_lshl_add_u64 v[132:133], v[132:133], 0, s[24:25]
	global_load_dword v127, v[132:133], off
	v_lshl_add_u64 v[132:133], v[132:133], 0, s[24:25]
	global_load_dword v128, v[132:133], off
	v_lshl_add_u64 v[132:133], v[132:133], 0, s[24:25]
	global_load_dword v129, v[132:133], off
	v_lshl_add_u64 v[132:133], v[132:133], 0, s[24:25]
	global_load_dword v130, v[132:133], off
	v_lshl_add_u64 v[132:133], v[132:133], 0, s[24:25]
	global_load_dword v131, v[132:133], off
	v_lshl_add_u64 v[132:133], v[132:133], 0, s[24:25]
	s_add_i32 s19, s19, -1
	s_waitcnt vmcnt(15)
	v_max_f32_e64 v18, v18, |v116|
	s_waitcnt vmcnt(14)
	v_max_f32_e64 v17, v17, |v117|
	s_waitcnt vmcnt(13)
	v_max_f32_e64 v18, v18, |v118|
	s_waitcnt vmcnt(12)
	v_max_f32_e64 v17, v17, |v119|
	s_waitcnt vmcnt(11)
	v_max_f32_e64 v18, v18, |v120|
	s_waitcnt vmcnt(10)
	v_max_f32_e64 v17, v17, |v121|
	s_waitcnt vmcnt(9)
	v_max_f32_e64 v18, v18, |v122|
	s_waitcnt vmcnt(8)
	v_max_f32_e64 v17, v17, |v123|
	s_waitcnt vmcnt(7)
	v_max_f32_e64 v18, v18, |v124|
	s_waitcnt vmcnt(6)
	v_max_f32_e64 v17, v17, |v125|
	s_waitcnt vmcnt(5)
	v_max_f32_e64 v18, v18, |v126|
	s_waitcnt vmcnt(4)
	v_max_f32_e64 v17, v17, |v127|
	s_waitcnt vmcnt(3)
	v_max_f32_e64 v18, v18, |v128|
	s_waitcnt vmcnt(2)
	v_max_f32_e64 v17, v17, |v129|
	s_waitcnt vmcnt(1)
	v_max_f32_e64 v18, v18, |v130|
	s_waitcnt vmcnt(0)
	v_max_f32_e64 v17, v17, |v131|
	s_cmp_lg_u32 s19, 0
	s_cbranch_scc1 .Lp1b_max
	v_max_f32_e32 v5, v17, v18

.LBB0_1503:
	s_nop 1
	v_mov_b32_e32 v4, 0
	v_mov_b32_e32 v5, 0
	v_mov_b32_e32 v6, 0
	v_mov_b32_e32 v7, 0
	s_and_saveexec_b64 s[12:13], s[4:5]
	s_cbranch_execz .LBB0_1502
	s_mov_b32 s22, 0xfffaee80
	s_mov_b32 s23, -1
	s_mov_b32 s24, 0x5680
	s_mov_b32 s25, 0
	v_lshl_add_u64 v[132:133], v[16:17], 0, s[22:23]
	global_load_dword v116, v[132:133], off
	v_lshl_add_u64 v[132:133], v[132:133], 0, s[24:25]
	global_load_dword v117, v[132:133], off
	v_lshl_add_u64 v[132:133], v[132:133], 0, s[24:25]
	global_load_dword v118, v[132:133], off
	v_lshl_add_u64 v[132:133], v[132:133], 0, s[24:25]
	global_load_dword v119, v[132:133], off
	v_lshl_add_u64 v[132:133], v[132:133], 0, s[24:25]
	global_load_dword v120, v[132:133], off
	v_lshl_add_u64 v[132:133], v[132:133], 0, s[24:25]
	global_load_dword v121, v[132:133], off
	v_lshl_add_u64 v[132:133], v[132:133], 0, s[24:25]
	global_load_dword v122, v[132:133], off
	v_lshl_add_u64 v[132:133], v[132:133], 0, s[24:25]
	global_load_dword v123, v[132:133], off
	v_lshl_add_u64 v[132:133], v[132:133], 0, s[24:25]
	global_load_dword v124, v[132:133], off
	v_lshl_add_u64 v[132:133], v[132:133], 0, s[24:25]
	global_load_dword v125, v[132:133], off
	v_lshl_add_u64 v[132:133], v[132:133], 0, s[24:25]
	global_load_dword v126, v[132:133], off
	v_lshl_add_u64 v[132:133], v[132:133], 0, s[24:25]
	global_load_dword v127, v[132:133], off
	v_lshl_add_u64 v[132:133], v[132:133], 0, s[24:25]
	global_load_dword v128, v[132:133], off
	v_lshl_add_u64 v[132:133], v[132:133], 0, s[24:25]
	global_load_dword v129, v[132:133], off
	v_lshl_add_u64 v[132:133], v[132:133], 0, s[24:25]
	global_load_dword v130, v[132:133], off
	v_lshl_add_u64 v[132:133], v[132:133], 0, s[24:25]
	global_load_dword v131, v[132:133], off
	s_waitcnt vmcnt(15)
	v_fmaak_f32 v134, v2, v116, 0x43000000
	v_cvt_pk_u8_f32 v4, v134, 0, 0
	s_waitcnt vmcnt(14)
	v_fmaak_f32 v134, v2, v117, 0x43000000
	v_cvt_pk_u8_f32 v4, v134, 1, v4
	s_waitcnt vmcnt(13)
	v_fmaak_f32 v134, v2, v118, 0x43000000
	v_cvt_pk_u8_f32 v4, v134, 2, v4
	s_waitcnt vmcnt(12)
	v_fmaak_f32 v134, v2, v119, 0x43000000
	v_cvt_pk_u8_f32 v4, v134, 3, v4
	v_xor_b32_e32 v4, 0x80808080, v4
	s_waitcnt vmcnt(11)
	v_fmaak_f32 v134, v2, v120, 0x43000000
	v_cvt_pk_u8_f32 v5, v134, 0, 0
	s_waitcnt vmcnt(10)
	v_fmaak_f32 v134, v2, v121, 0x43000000
	v_cvt_pk_u8_f32 v5, v134, 1, v5
	s_waitcnt vmcnt(9)
	v_fmaak_f32 v134, v2, v122, 0x43000000
	v_cvt_pk_u8_f32 v5, v134, 2, v5
	s_waitcnt vmcnt(8)
	v_fmaak_f32 v134, v2, v123, 0x43000000
	v_cvt_pk_u8_f32 v5, v134, 3, v5
	v_xor_b32_e32 v5, 0x80808080, v5
	s_waitcnt vmcnt(7)
	v_fmaak_f32 v134, v2, v124, 0x43000000
	v_cvt_pk_u8_f32 v6, v134, 0, 0
	s_waitcnt vmcnt(6)
	v_fmaak_f32 v134, v2, v125, 0x43000000
	v_cvt_pk_u8_f32 v6, v134, 1, v6
	s_waitcnt vmcnt(5)
	v_fmaak_f32 v134, v2, v126, 0x43000000
	v_cvt_pk_u8_f32 v6, v134, 2, v6
	s_waitcnt vmcnt(4)
	v_fmaak_f32 v134, v2, v127, 0x43000000
	v_cvt_pk_u8_f32 v6, v134, 3, v6
	v_xor_b32_e32 v6, 0x80808080, v6
	s_waitcnt vmcnt(3)
	v_fmaak_f32 v134, v2, v128, 0x43000000
	v_cvt_pk_u8_f32 v7, v134, 0, 0
	s_waitcnt vmcnt(2)
	v_fmaak_f32 v134, v2, v129, 0x43000000
	v_cvt_pk_u8_f32 v7, v134, 1, v7
	s_waitcnt vmcnt(1)
	v_fmaak_f32 v134, v2, v130, 0x43000000
	v_cvt_pk_u8_f32 v7, v134, 2, v7
	s_waitcnt vmcnt(0)
	v_fmaak_f32 v134, v2, v131, 0x43000000
	v_cvt_pk_u8_f32 v7, v134, 3, v7
	v_xor_b32_e32 v7, 0x80808080, v7
	s_branch .LBB0_1502
